# MLA side-job tick: phase 1 (LDS writes) dispatched straight from the tick head, skipping the tile addressing SALU chain
# baseline (speedup 1.0000x reference)
; #define LAS __attribute__((address_space(3)))
; DEV void sj_tick(const Params& p, int layer, SideJob& sj, LAS char* lds, int tid) {
;     LAS float* tile = (LAS float*)(lds + SJ_TILE_OFF);
;     const int ph = sj.g & 3; ++sj.g;
;     if (sj.le >= 64 || ph == 3) return;
;     const SjDesc d = sj_desc(p, layer, sj.le, sj.j);
;     if (ph == 0) {
;         const int krow = tid >> 4, c4 = (tid & 15) * 4;
;         const float* a0 = (d.mode == 0 || d.mode == 2) ? d.s0 + (size_t)(d.k0 + krow) * d.ld + d.nt * 64 + c4
;                                         : ((c4 < 32) ? d.s0 + (size_t)(d.k0 + krow) * 512 + d.nt * 32 + c4 : d.s1 + (size_t)(d.k0 + krow) * 512 + d.nt * 32 + c4 - 32);
;         sj.v0 = *(const f32x4*)a0; sj.v1 = *(const f32x4*)(a0 + (size_t)32 * d.ld);
.LBB0_813:
	s_mov_b32 s100, 0
	s_add_i32 s2, s29, s61
	s_and_b32 s63, s2, 3
	s_cmp_gt_i32 s33, 63
	s_cselect_b64 s[8:9], -1, 0
	s_cmp_eq_u32 s63, 3
	s_cselect_b64 s[20:21], -1, 0
	s_or_b64 s[8:9], s[8:9], s[20:21]
	s_and_b64 vcc, exec, s[8:9]
	s_cbranch_vccnz .LBB0_812
	s_cmp_eq_u32 s63, 1
	s_cbranch_scc1 .Lmla_t1
	s_add_i32 s20, s33, s12
	s_cmpk_lt_i32 s36, 0x100
	s_cselect_b64 s[50:51], -1, 0
	s_lshl_b32 s58, s36, 6
	s_cmpk_gt_i32 s36, 0xff
	s_mov_b64 s[56:57], -1
	s_cbranch_scc1 .LBB0_816
	s_ashr_i32 s21, s20, 31
	s_lshl_b64 s[52:53], s[20:21], 21
	s_add_u32 s8, s44, s52
	s_addc_u32 s9, s45, s53
	s_add_u32 s52, s46, s52
	s_addc_u32 s53, s47, s53
	s_lshl_b64 s[54:55], s[20:21], 20
	s_add_u32 s54, s13, s54
	s_addc_u32 s55, s16, s55
	s_and_b32 s30, s58, 0x3c0
	s_ashr_i32 s64, s36, 4
	s_mov_b64 s[56:57], 0

; #define LAS __attribute__((address_space(3)))
; DEV void sj_tick(const Params& p, int layer, SideJob& sj, LAS char* lds, int tid) {
;     ...
;     } else if (ph == 1) {
;         const int krow = tid >> 4, c4 = (tid & 15) * 4;
;         LAS float* t0 = tile + krow * 65 + c4; LAS float* t1 = t0 + 32 * 65;
;         t0[0] = sj.v0[0]; t0[1] = sj.v0[1]; t0[2] = sj.v0[2]; t0[3] = sj.v0[3]; t1[0] = sj.v1[0]; t1[1] = sj.v1[1]; t1[2] = sj.v1[2]; t1[3] = sj.v1[3];
.Lmla_t1:
	v_add_u32_e32 v98, 0x2080, v194
	s_waitcnt vmcnt(4)
	ds_write2_b32 v194, v182, v183 offset1:1
	ds_write2_b32 v194, v184, v185 offset0:2 offset1:3
	s_waitcnt vmcnt(3)
	ds_write2_b32 v98, v186, v187 offset1:1
	v_add_u32_e32 v98, 0x2088, v194
	ds_write2_b32 v98, v188, v189 offset1:1
	s_branch .LBB0_812
